# out-projection epilogue: residual rows of three more row groups (layer 1: all remaining) requested right behind the initial batch into registers dead in the epilogue; all vmcnt waits recomputed
# baseline (speedup 1.0000x reference)
.LBB0_880:
	s_lshl_b32 s15, s89, 8
	s_or_b32 s89, s15, s72
	s_lshl_b32 s15, s90, 8
	s_ashr_i32 s14, s90, 4
	s_add_i32 s15, s15, s69
	s_cmp_lt_i32 s90, 64
	v_mbcnt_lo_u32_b32 v129, -1, 0
	v_mbcnt_hi_u32_b32 v129, -1, v129
	s_cselect_b64 vcc, -1, 0
	s_mul_i32 s90, s14, 0x3000
	s_mul_hi_i32 s91, s14, 0x3000
	v_and_or_b32 v148, v129, 15, s15
	s_and_b64 s[14:15], vcc, exec
	v_ashrrev_i32_e32 v129, 1, v129
	s_cselect_b32 s15, s91, 0
	s_cselect_b32 s14, s90, 0xc000
	v_and_b32_e32 v129, -8, v129
	v_add_u32_e32 v194, s89, v129
	s_cselect_b32 s90, s18, s20
	s_cselect_b32 s91, s19, s21
	s_lshl_b64 s[14:15], s[14:15], 2
	v_add_u32_e32 v128, 0xffffc000, v148
	s_add_u32 s14, s16, s14
	v_ashrrev_i32_e32 v195, 31, v194
	v_cndmask_b32_e32 v128, v128, v148, vcc
	s_addc_u32 s15, s17, s15
	v_lshlrev_b64 v[136:137], 2, v[194:195]
	v_lshl_add_u64 v[130:131], s[14:15], 0, v[136:137]
	s_mov_b64 s[14:15], 0x104000
	v_ashrrev_i32_e32 v129, 31, v128
	v_lshl_add_u64 v[138:139], v[130:131], 0, s[14:15]
	v_lshlrev_b64 v[128:129], 13, v[128:129]
	s_mov_b32 s14, 0x104000
	v_lshl_add_u64 v[140:141], s[90:91], 0, v[128:129]
	v_add_co_u32_e32 v128, vcc, s14, v130
	v_lshl_add_u64 v[150:151], v[140:141], 0, v[136:137]
	s_nop 0
	v_addc_co_u32_e32 v129, vcc, 0, v131, vcc
	v_add_co_u32_e32 v186, vcc, s11, v150
	s_mov_b64 s[14:15], 0x20000
	global_load_dwordx4 v[132:135], v[128:129], off
	s_nop 0
	global_load_dwordx4 v[128:131], v[138:139], off offset:528
	global_load_dwordx4 v[144:147], v[150:151], off offset:16 nt
	global_load_dwordx4 v[166:169], v[150:151], off nt
	global_load_dwordx4 v[140:143], v[138:139], off offset:16
	s_nop 0
	global_load_dwordx4 v[136:139], v[138:139], off offset:512
	s_nop 0
	global_load_dwordx4 v[170:173], v[150:151], off offset:528 nt
	global_load_dwordx4 v[174:177], v[150:151], off offset:512 nt
	v_addc_co_u32_e32 v187, vcc, 0, v151, vcc
	v_lshl_add_u64 v[182:183], v[150:151], 0, s[14:15]
	s_mov_b64 s[14:15], 0x20200
	global_load_dwordx4 v[178:181], v[186:187], off nt
	v_lshl_add_u64 v[190:191], v[150:151], 0, s[14:15]
	global_load_dwordx4 v[182:185], v[182:183], off offset:16 nt
	s_nop 0
	global_load_dwordx4 v[186:189], v[186:187], off offset:512 nt
	v_ashrrev_i32_e32 v149, 31, v148
	global_load_dwordx4 v[190:193], v[190:191], off offset:16 nt
	s_mov_b64 s[14:15], 0x40200
	v_lshl_add_u64 v[252:253], v[150:151], 0, s[14:15]
	global_load_dwordx4 v[200:203], v[252:253], off offset:16 nt
	s_mov_b32 s14, 0x40000
	v_add_co_u32_e32 v252, vcc, s14, v150
	s_nop 1
	v_addc_co_u32_e32 v253, vcc, 0, v151, vcc
	global_load_dwordx4 v[204:207], v[252:253], off nt
	global_load_dwordx4 v[208:211], v[252:253], off offset:512 nt
	s_mov_b64 s[14:15], 0x40000
	v_lshl_add_u64 v[252:253], v[150:151], 0, s[14:15]
	global_load_dwordx4 v[212:215], v[252:253], off offset:16 nt
	s_mov_b32 s14, 0x60000
	v_add_co_u32_e32 v252, vcc, s14, v150
	s_nop 1
	v_addc_co_u32_e32 v253, vcc, 0, v151, vcc
	global_load_dwordx4 v[216:219], v[252:253], off nt
	s_mov_b64 s[14:15], 0x60000
	v_lshl_add_u64 v[252:253], v[150:151], 0, s[14:15]
	global_load_dwordx4 v[220:223], v[252:253], off offset:16 nt
	s_mov_b32 s14, 0x60000
	v_add_co_u32_e32 v252, vcc, s14, v150
	s_nop 1
	v_addc_co_u32_e32 v253, vcc, 0, v151, vcc
	global_load_dwordx4 v[224:227], v[252:253], off offset:512 nt
	s_mov_b64 s[14:15], 0x60200
	v_lshl_add_u64 v[252:253], v[150:151], 0, s[14:15]
	global_load_dwordx4 v[228:231], v[252:253], off offset:16 nt
	v_lshl_add_u64 v[252:253], v[150:151], 0, s[28:29]
	global_load_dwordx4 v[232:235], v[252:253], off offset:16 nt
	v_add_co_u32_e32 v252, vcc, s76, v150
	s_nop 1
	v_addc_co_u32_e32 v253, vcc, 0, v151, vcc
	global_load_dwordx4 v[236:239], v[252:253], off nt
	global_load_dwordx4 v[240:243], v[252:253], off offset:512 nt
	v_lshl_add_u64 v[252:253], v[150:151], 0, s[30:31]
	global_load_dwordx4 v[244:247], v[252:253], off offset:16 nt
	s_mov_b32 s89, 0x40000
	v_lshlrev_b64 v[148:149], 12, v[148:149]
	s_mov_b64 s[14:15], 0x40200
	v_lshl_add_u64 v[148:149], s[24:25], 0, v[148:149]
	v_add_co_u32_e32 v196, vcc, s89, v150
	v_lshl_add_u64 v[148:149], v[194:195], 1, v[148:149]
	v_lshl_add_u64 v[194:195], v[150:151], 0, s[14:15]
	v_addc_co_u32_e32 v197, vcc, 0, v151, vcc
	s_mov_b32 s14, 0x10000
	s_mov_b64 s[90:91], 0x40000
	v_lshl_add_u64 v[198:199], v[150:151], 0, s[90:91]
	s_waitcnt vmcnt(19)
	v_pk_fma_f32 v[122:123], v[122:123], v[142:143], v[146:147]
	v_pk_fma_f32 v[124:125], v[124:125], v[132:133], v[166:167]
	v_pk_fma_f32 v[126:127], v[126:127], v[134:135], v[168:169]
	v_pk_fma_f32 v[120:121], v[120:121], v[140:141], v[144:145]
	s_waitcnt vmcnt(16)
	v_pk_fma_f32 v[110:111], v[110:111], v[138:139], v[176:177]
	v_pk_fma_f32 v[108:109], v[108:109], v[136:137], v[174:175]
	v_pk_fma_f32 v[144:145], v[106:107], v[130:131], v[172:173]
	v_pk_fma_f32 v[146:147], v[104:105], v[128:129], v[170:171]
	v_cvt_pk_bf16_f32 v104, v124, v125
	v_cvt_pk_bf16_f32 v105, v126, v127
	v_cvt_pk_bf16_f32 v106, v120, v121
	v_cvt_pk_bf16_f32 v107, v122, v123
	v_add_co_u32_e32 v124, vcc, s14, v148
	s_waitcnt vmcnt(15)
	v_pk_fma_f32 v[118:119], v[118:119], v[134:135], v[180:181]
	v_pk_fma_f32 v[116:117], v[116:117], v[132:133], v[178:179]
	s_waitcnt vmcnt(14)
	v_pk_fma_f32 v[166:167], v[114:115], v[142:143], v[184:185]
	v_pk_fma_f32 v[114:115], v[112:113], v[140:141], v[182:183]
	v_cvt_pk_bf16_f32 v108, v108, v109
	v_cvt_pk_bf16_f32 v109, v110, v111
	v_cvt_pk_bf16_f32 v110, v146, v147
	v_cvt_pk_bf16_f32 v111, v144, v145
	v_cvt_pk_bf16_f32 v112, v116, v117
	v_cvt_pk_bf16_f32 v113, v118, v119
	global_store_dwordx4 v[148:149], v[104:107], off
	global_store_dwordx4 v[148:149], v[108:111], off offset:256
	v_addc_co_u32_e32 v125, vcc, 0, v149, vcc
	v_cvt_pk_bf16_f32 v114, v114, v115
	v_cvt_pk_bf16_f32 v115, v166, v167
	s_mov_b32 s14, 0x60000
	global_store_dwordx4 v[124:125], v[112:115], off
	s_waitcnt vmcnt(16)
	v_pk_fma_f32 v[100:101], v[100:101], v[136:137], v[186:187]
	v_pk_fma_f32 v[102:103], v[102:103], v[138:139], v[188:189]
	s_waitcnt vmcnt(15)
	v_pk_fma_f32 v[112:113], v[98:99], v[130:131], v[192:193]
	v_pk_fma_f32 v[98:99], v[96:97], v[128:129], v[190:191]
	v_cvt_pk_bf16_f32 v96, v100, v101
	v_cvt_pk_bf16_f32 v97, v102, v103
	v_lshl_add_u64 v[166:167], v[150:151], 0, s[28:29]
	v_cvt_pk_bf16_f32 v98, v98, v99
	v_cvt_pk_bf16_f32 v99, v112, v113
	v_add_co_u32_e32 v112, vcc, s14, v150
	s_mov_b64 s[14:15], 0x60000
	v_lshl_add_u64 v[100:101], v[150:151], 0, s[14:15]
	s_mov_b64 s[14:15], 0x60200
	global_store_dwordx4 v[124:125], v[96:99], off offset:256
	v_addc_co_u32_e32 v113, vcc, 0, v151, vcc
	v_lshl_add_u64 v[124:125], v[150:151], 0, s[14:15]
	s_nop 0
	s_nop 0
	v_add_co_u32_e32 v144, vcc, s11, v148
	s_nop 0
	v_addc_co_u32_e32 v145, vcc, 0, v149, vcc
	v_add_co_u32_e32 v146, vcc, s77, v148
	v_lshl_add_u64 v[170:171], v[150:151], 0, s[30:31]
	s_nop 0
	v_addc_co_u32_e32 v147, vcc, 0, v149, vcc
	v_add_co_u32_e32 v168, vcc, s76, v150
	s_waitcnt vmcnt(15)
	v_pk_fma_f32 v[106:107], v[74:75], v[130:131], v[202:203]
	v_addc_co_u32_e32 v169, vcc, 0, v151, vcc
	s_waitcnt vmcnt(14)
	v_pk_fma_f32 v[94:95], v[94:95], v[134:135], v[206:207]
	v_pk_fma_f32 v[92:93], v[92:93], v[132:133], v[204:205]
	s_waitcnt vmcnt(12)
	v_pk_fma_f32 v[90:91], v[90:91], v[142:143], v[214:215]
	v_pk_fma_f32 v[88:89], v[88:89], v[140:141], v[212:213]
	v_pk_fma_f32 v[78:79], v[78:79], v[138:139], v[210:211]
	v_pk_fma_f32 v[76:77], v[76:77], v[136:137], v[208:209]
	v_pk_fma_f32 v[104:105], v[72:73], v[128:129], v[200:201]
	v_cvt_pk_bf16_f32 v72, v92, v93
	v_cvt_pk_bf16_f32 v73, v94, v95
	v_cvt_pk_bf16_f32 v74, v88, v89
	v_cvt_pk_bf16_f32 v75, v90, v91
	v_add_co_u32_e32 v172, vcc, s78, v150
	v_cvt_pk_bf16_f32 v76, v76, v77
	v_cvt_pk_bf16_f32 v77, v78, v79
	v_cvt_pk_bf16_f32 v78, v104, v105
	v_cvt_pk_bf16_f32 v79, v106, v107
	global_store_dwordx4 v[144:145], v[72:75], off
	global_store_dwordx4 v[144:145], v[76:79], off offset:256
	v_addc_co_u32_e32 v173, vcc, 0, v151, vcc
	v_lshl_add_u64 v[104:105], v[150:151], 0, s[40:41]
	s_waitcnt vmcnt(13)
	v_pk_fma_f32 v[86:87], v[86:87], v[134:135], v[218:219]
	v_pk_fma_f32 v[88:89], v[84:85], v[132:133], v[216:217]
	s_waitcnt vmcnt(12)
	v_pk_fma_f32 v[90:91], v[82:83], v[142:143], v[222:223]
	v_pk_fma_f32 v[92:93], v[80:81], v[140:141], v[220:221]
	s_waitcnt vmcnt(10)
	v_pk_fma_f32 v[96:97], v[66:67], v[130:131], v[230:231]
	v_pk_fma_f32 v[98:99], v[64:65], v[128:129], v[228:229]
	v_cvt_pk_bf16_f32 v64, v88, v89
	v_cvt_pk_bf16_f32 v65, v86, v87
	v_cvt_pk_bf16_f32 v66, v92, v93
	v_cvt_pk_bf16_f32 v67, v90, v91
	v_pk_fma_f32 v[94:95], v[70:71], v[138:139], v[226:227]
	v_pk_fma_f32 v[68:69], v[68:69], v[136:137], v[224:225]
	v_cvt_pk_bf16_f32 v87, v94, v95
	v_cvt_pk_bf16_f32 v88, v98, v99
	v_cvt_pk_bf16_f32 v89, v96, v97
	v_lshl_add_u64 v[100:101], v[150:151], 0, s[38:39]
	v_cvt_pk_bf16_f32 v86, v68, v69
	global_store_dwordx4 v[146:147], v[64:67], off
	global_store_dwordx4 v[146:147], v[86:89], off offset:256
	global_load_dwordx4 v[64:67], v[172:173], off nt
	v_lshl_add_u64 v[68:69], v[150:151], 0, s[34:35]
	global_load_dwordx4 v[86:89], v[68:69], off offset:16 nt
	global_load_dwordx4 v[90:93], v[172:173], off offset:512 nt
	v_lshl_add_u64 v[68:69], v[150:151], 0, s[36:37]
	global_load_dwordx4 v[94:97], v[68:69], off offset:16 nt
	v_add_co_u32_e32 v68, vcc, s79, v148
	s_waitcnt vmcnt(15)
	v_pk_fma_f32 v[72:73], v[42:43], v[130:131], v[234:235]
	v_addc_co_u32_e32 v69, vcc, 0, v149, vcc
	v_add_co_u32_e32 v98, vcc, s81, v148
	s_waitcnt vmcnt(13)
	v_pk_fma_f32 v[46:47], v[46:47], v[138:139], v[242:243]
	v_addc_co_u32_e32 v99, vcc, 0, v149, vcc
	v_add_co_u32_e32 v102, vcc, s80, v150
	v_pk_fma_f32 v[44:45], v[44:45], v[136:137], v[240:241]
	s_nop 0
	v_addc_co_u32_e32 v103, vcc, 0, v151, vcc
	v_pk_fma_f32 v[62:63], v[62:63], v[134:135], v[238:239]
	v_pk_fma_f32 v[60:61], v[60:61], v[132:133], v[236:237]
	s_waitcnt vmcnt(12)
	v_pk_fma_f32 v[58:59], v[58:59], v[142:143], v[246:247]
	v_pk_fma_f32 v[56:57], v[56:57], v[140:141], v[244:245]
	v_pk_fma_f32 v[70:71], v[40:41], v[128:129], v[232:233]
	v_cvt_pk_bf16_f32 v40, v60, v61
	v_cvt_pk_bf16_f32 v41, v62, v63
	v_cvt_pk_bf16_f32 v42, v56, v57
	v_cvt_pk_bf16_f32 v43, v58, v59
	v_cvt_pk_bf16_f32 v44, v44, v45
	v_cvt_pk_bf16_f32 v45, v46, v47
	s_nop 0
	v_cvt_pk_bf16_f32 v46, v70, v71
	v_cvt_pk_bf16_f32 v47, v72, v73
	s_waitcnt vmcnt(3)
	v_pk_fma_f32 v[52:53], v[52:53], v[132:133], v[64:65]
	v_add_co_u32_e32 v106, vcc, s82, v150
	v_pk_fma_f32 v[54:55], v[54:55], v[134:135], v[66:67]
	s_waitcnt vmcnt(2)
	v_pk_fma_f32 v[56:57], v[50:51], v[142:143], v[88:89]
	v_pk_fma_f32 v[58:59], v[48:49], v[140:141], v[86:87]
	s_waitcnt vmcnt(1)
	v_pk_fma_f32 v[60:61], v[38:39], v[138:139], v[92:93]
	v_pk_fma_f32 v[62:63], v[36:37], v[136:137], v[90:91]
	global_store_dwordx4 v[68:69], v[40:43], off
	global_store_dwordx4 v[68:69], v[44:47], off offset:256
	v_addc_co_u32_e32 v107, vcc, 0, v151, vcc
	s_nop 0
	v_cvt_pk_bf16_f32 v44, v52, v53
	v_cvt_pk_bf16_f32 v45, v54, v55
	v_cvt_pk_bf16_f32 v46, v58, v59
	v_cvt_pk_bf16_f32 v47, v56, v57
	v_cvt_pk_bf16_f32 v52, v62, v63
	v_cvt_pk_bf16_f32 v53, v60, v61
	global_load_dwordx4 v[36:39], v[102:103], off nt
	global_load_dwordx4 v[40:43], v[100:101], off offset:16 nt
	s_waitcnt vmcnt(4)
	v_pk_fma_f32 v[64:65], v[34:35], v[130:131], v[96:97]
	v_pk_fma_f32 v[66:67], v[32:33], v[128:129], v[94:95]
	global_load_dwordx4 v[32:35], v[102:103], off offset:512 nt
	global_load_dwordx4 v[48:51], v[104:105], off offset:16 nt
	v_cvt_pk_bf16_f32 v54, v66, v67
	v_cvt_pk_bf16_f32 v55, v64, v65
	global_store_dwordx4 v[98:99], v[44:47], off
	global_store_dwordx4 v[98:99], v[52:55], off offset:256
	v_lshl_add_u64 v[60:61], v[150:151], 0, s[44:45]
	global_load_dwordx4 v[44:47], v[106:107], off nt
	v_lshl_add_u64 v[52:53], v[150:151], 0, s[42:43]
	global_load_dwordx4 v[52:55], v[52:53], off offset:16 nt
	s_nop 0
	global_load_dwordx4 v[56:59], v[106:107], off offset:512 nt
	v_add_co_u32_e32 v64, vcc, s83, v148
	global_load_dwordx4 v[60:63], v[60:61], off offset:16 nt
	s_nop 0
	v_addc_co_u32_e32 v65, vcc, 0, v149, vcc
	v_add_co_u32_e32 v66, vcc, s84, v148
	s_waitcnt vmcnt(9)
	v_pk_fma_f32 v[30:31], v[30:31], v[134:135], v[38:39]
	v_addc_co_u32_e32 v67, vcc, 0, v149, vcc
	s_waitcnt vmcnt(8)
	v_pk_fma_f32 v[26:27], v[26:27], v[142:143], v[42:43]
	v_pk_fma_f32 v[24:25], v[24:25], v[140:141], v[40:41]
	s_andn2_b64 vcc, exec, s[4:5]
	v_pk_fma_f32 v[28:29], v[28:29], v[132:133], v[36:37]
	s_waitcnt vmcnt(7)
	v_pk_fma_f32 v[14:15], v[14:15], v[138:139], v[34:35]
	v_pk_fma_f32 v[12:13], v[12:13], v[136:137], v[32:33]
	s_waitcnt vmcnt(6)
	v_pk_fma_f32 v[32:33], v[10:11], v[130:131], v[50:51]
	v_pk_fma_f32 v[34:35], v[8:9], v[128:129], v[48:49]
	v_cvt_pk_bf16_f32 v8, v28, v29
	v_cvt_pk_bf16_f32 v9, v30, v31
	v_cvt_pk_bf16_f32 v10, v24, v25
	v_cvt_pk_bf16_f32 v11, v26, v27
	s_waitcnt vmcnt(3)
	v_pk_fma_f32 v[22:23], v[22:23], v[134:135], v[46:47]
	v_pk_fma_f32 v[20:21], v[20:21], v[132:133], v[44:45]
	s_waitcnt vmcnt(2)
	v_pk_fma_f32 v[18:19], v[18:19], v[142:143], v[54:55]
	v_pk_fma_f32 v[16:17], v[16:17], v[140:141], v[52:53]
	s_waitcnt vmcnt(1)
	v_pk_fma_f32 v[6:7], v[6:7], v[138:139], v[58:59]
	v_pk_fma_f32 v[4:5], v[4:5], v[136:137], v[56:57]
	s_waitcnt vmcnt(0)
	v_pk_fma_f32 v[24:25], v[2:3], v[130:131], v[62:63]
	v_pk_fma_f32 v[26:27], v[0:1], v[128:129], v[60:61]
	v_cvt_pk_bf16_f32 v0, v20, v21
	v_cvt_pk_bf16_f32 v1, v22, v23
	v_cvt_pk_bf16_f32 v2, v16, v17
	v_cvt_pk_bf16_f32 v3, v18, v19
	s_mov_b64 s[4:5], -1
	v_cvt_pk_bf16_f32 v12, v12, v13
	v_cvt_pk_bf16_f32 v13, v14, v15
	v_cvt_pk_bf16_f32 v14, v34, v35
	v_cvt_pk_bf16_f32 v15, v32, v33
	global_store_dwordx4 v[64:65], v[8:11], off
	global_store_dwordx4 v[64:65], v[12:15], off offset:256
	v_cvt_pk_bf16_f32 v4, v4, v5
	v_cvt_pk_bf16_f32 v5, v6, v7
	v_cvt_pk_bf16_f32 v6, v26, v27
	v_cvt_pk_bf16_f32 v7, v24, v25
	global_store_dwordx4 v[66:67], v[0:3], off
	global_store_dwordx4 v[66:67], v[4:7], off offset:256
	s_cbranch_vccnz .LBB0_873
	s_andn2_b64 vcc, exec, s[22:23]
	s_cbranch_vccnz .LBB0_872
	s_barrier
	s_branch .LBB0_872

.LBB0_2143:
	s_lshl_b32 s15, s68, 8
	s_lshl_b32 s14, s69, 8
	s_add_i32 s15, s15, s49
	v_mbcnt_lo_u32_b32 v129, -1, 0
	v_mbcnt_hi_u32_b32 v129, -1, v129
	s_or_b32 s14, s14, s50
	v_ashrrev_i32_e32 v128, 1, v129
	v_and_b32_e32 v128, -8, v128
	v_and_or_b32 v130, v129, 15, s15
	v_add_u32_e32 v128, s14, v128
	v_ashrrev_i32_e32 v131, 31, v130
	v_ashrrev_i32_e32 v129, 31, v128
	v_lshlrev_b64 v[144:145], 12, v[130:131]
	s_ashr_i32 s14, s68, 4
	v_lshl_add_u64 v[130:131], s[24:25], 0, v[144:145]
	v_lshlrev_b64 v[146:147], 1, v[128:129]
	s_mul_hi_i32 s15, s14, 0xc000
	s_mul_i32 s14, s14, 0xc000
	v_lshl_add_u64 v[158:159], v[130:131], 0, v[146:147]
	s_add_u32 s14, s16, s14
	v_add_co_u32_e32 v130, vcc, s42, v158
	s_addc_u32 s15, s17, s15
	s_nop 0
	v_addc_co_u32_e32 v131, vcc, 0, v159, vcc
	v_lshl_add_u64 v[128:129], v[128:129], 2, s[14:15]
	global_load_dwordx4 v[152:155], v[158:159], off nt
	global_load_dwordx4 v[174:177], v[158:159], off offset:256 nt
	global_load_dwordx4 v[178:181], v[130:131], off nt
	global_load_dwordx4 v[182:185], v[130:131], off offset:256 nt
	v_add_co_u32_e32 v130, vcc, s58, v128
	v_lshl_add_u64 v[144:145], s[20:21], 0, v[144:145]
	s_nop 0
	v_addc_co_u32_e32 v131, vcc, 0, v129, vcc
	global_load_dwordx4 v[140:143], v[130:131], off
	v_lshl_add_u64 v[128:129], v[128:129], 0, s[26:27]
	global_load_dwordx4 v[136:139], v[128:129], off offset:16
	global_load_dwordx4 v[132:135], v[128:129], off offset:512
	s_nop 0
	global_load_dwordx4 v[128:131], v[128:129], off offset:528
	v_add_co_u32_e32 v148, vcc, s11, v158
	v_lshl_add_u64 v[156:157], v[144:145], 0, v[146:147]
	s_nop 0
	v_addc_co_u32_e32 v149, vcc, 0, v159, vcc
	global_load_dwordx4 v[186:189], v[148:149], off offset:256 nt
	global_load_dwordx4 v[190:193], v[148:149], off nt
	v_add_co_u32_e32 v252, vcc, s59, v158
	s_nop 1
	v_addc_co_u32_e32 v253, vcc, 0, v159, vcc
	global_load_dwordx4 v[210:213], v[252:253], off nt
	global_load_dwordx4 v[214:217], v[252:253], off offset:256 nt
	v_add_co_u32_e32 v252, vcc, s60, v158
	s_nop 1
	v_addc_co_u32_e32 v253, vcc, 0, v159, vcc
	global_load_dwordx4 v[218:221], v[252:253], off offset:256 nt
	global_load_dwordx4 v[222:225], v[252:253], off nt
	v_add_co_u32_e32 v252, vcc, s61, v158
	s_nop 1
	v_addc_co_u32_e32 v253, vcc, 0, v159, vcc
	global_load_dwordx4 v[226:229], v[252:253], off nt
	global_load_dwordx4 v[230:233], v[252:253], off offset:256 nt
	v_add_co_u32_e32 v252, vcc, s62, v158
	s_nop 1
	v_addc_co_u32_e32 v253, vcc, 0, v159, vcc
	global_load_dwordx4 v[234:237], v[252:253], off offset:256 nt
	global_load_dwordx4 v[238:241], v[252:253], off nt
	v_add_co_u32_e32 v252, vcc, s63, v158
	s_nop 1
	v_addc_co_u32_e32 v253, vcc, 0, v159, vcc
	global_load_dwordx4 v[242:245], v[252:253], off nt
	global_load_dwordx4 v[246:249], v[252:253], off offset:256 nt
	v_add_co_u32_e32 v144, vcc, s59, v158
	s_waitcnt vmcnt(19)
	v_lshlrev_b32_e32 v194, 16, v152
	v_and_b32_e32 v195, 0xffff0000, v152
	v_lshlrev_b32_e32 v152, 16, v153
	v_and_b32_e32 v153, 0xffff0000, v153
	v_lshlrev_b32_e32 v196, 16, v154
	v_and_b32_e32 v197, 0xffff0000, v154
	v_lshlrev_b32_e32 v154, 16, v155
	v_and_b32_e32 v155, 0xffff0000, v155
	s_waitcnt vmcnt(18)
	v_lshlrev_b32_e32 v198, 16, v174
	v_and_b32_e32 v199, 0xffff0000, v174
	v_addc_co_u32_e32 v145, vcc, 0, v159, vcc
	v_lshlrev_b32_e32 v200, 16, v176
	v_and_b32_e32 v201, 0xffff0000, v176
	v_lshlrev_b32_e32 v176, 16, v177
	v_and_b32_e32 v177, 0xffff0000, v177
	s_waitcnt vmcnt(15)
	v_pk_fma_f32 v[126:127], v[126:127], v[142:143], v[152:153]
	v_pk_fma_f32 v[124:125], v[124:125], v[140:141], v[194:195]
	s_waitcnt vmcnt(14)
	v_pk_fma_f32 v[152:153], v[122:123], v[138:139], v[154:155]
	v_pk_fma_f32 v[122:123], v[120:121], v[136:137], v[196:197]
	v_cvt_pk_bf16_f32 v120, v124, v125
	v_cvt_pk_bf16_f32 v121, v126, v127
	s_waitcnt vmcnt(13)
	v_pk_fma_f32 v[116:117], v[116:117], v[132:133], v[198:199]
	s_nop 0
	v_lshlrev_b32_e32 v202, 16, v178
	v_and_b32_e32 v203, 0xffff0000, v178
	v_cvt_pk_bf16_f32 v122, v122, v123
	v_cvt_pk_bf16_f32 v123, v152, v153
	global_store_dwordx4 v[156:157], v[120:123], off
	v_lshlrev_b32_e32 v174, 16, v175
	v_and_b32_e32 v175, 0xffff0000, v175
	s_waitcnt vmcnt(13)
	v_pk_fma_f32 v[120:121], v[114:115], v[130:131], v[176:177]
	v_pk_fma_f32 v[114:115], v[112:113], v[128:129], v[200:201]
	v_cvt_pk_bf16_f32 v112, v116, v117
	v_add_co_u32_e32 v116, vcc, s60, v158
	v_lshlrev_b32_e32 v178, 16, v179
	v_and_b32_e32 v179, 0xffff0000, v179
	v_lshlrev_b32_e32 v204, 16, v180
	v_and_b32_e32 v205, 0xffff0000, v180
	v_lshlrev_b32_e32 v180, 16, v181
	v_and_b32_e32 v181, 0xffff0000, v181
	v_addc_co_u32_e32 v117, vcc, 0, v159, vcc
	v_pk_fma_f32 v[108:109], v[108:109], v[140:141], v[202:203]
	v_lshlrev_b32_e32 v206, 16, v182
	v_and_b32_e32 v207, 0xffff0000, v182
	v_pk_fma_f32 v[118:119], v[118:119], v[134:135], v[174:175]
	v_cvt_pk_bf16_f32 v114, v114, v115
	v_cvt_pk_bf16_f32 v115, v120, v121
	v_pk_fma_f32 v[110:111], v[110:111], v[142:143], v[178:179]
	v_cvt_pk_bf16_f32 v113, v118, v119
	v_pk_fma_f32 v[178:179], v[106:107], v[138:139], v[180:181]
	v_pk_fma_f32 v[106:107], v[104:105], v[136:137], v[204:205]
	v_cvt_pk_bf16_f32 v104, v108, v109
	v_add_co_u32_e32 v108, vcc, s42, v156
	v_lshlrev_b32_e32 v208, 16, v184
	v_and_b32_e32 v209, 0xffff0000, v184
	v_lshlrev_b32_e32 v184, 16, v185
	v_and_b32_e32 v185, 0xffff0000, v185
	global_store_dwordx4 v[156:157], v[112:115], off offset:256
	v_cvt_pk_bf16_f32 v105, v110, v111
	v_addc_co_u32_e32 v109, vcc, 0, v157, vcc
	v_pk_fma_f32 v[100:101], v[100:101], v[132:133], v[206:207]
	v_lshlrev_b32_e32 v182, 16, v183
	v_and_b32_e32 v183, 0xffff0000, v183
	v_cvt_pk_bf16_f32 v106, v106, v107
	v_cvt_pk_bf16_f32 v107, v178, v179
	global_store_dwordx4 v[108:109], v[104:107], off
	v_pk_fma_f32 v[102:103], v[102:103], v[134:135], v[182:183]
	s_waitcnt vmcnt(13)
	v_and_b32_e32 v177, 0xffff0000, v190
	v_pk_fma_f32 v[104:105], v[98:99], v[130:131], v[184:185]
	v_pk_fma_f32 v[98:99], v[96:97], v[128:129], v[208:209]
	v_cvt_pk_bf16_f32 v96, v100, v101
	v_add_co_u32_e32 v100, vcc, s61, v158
	v_cvt_pk_bf16_f32 v97, v102, v103
	v_cvt_pk_bf16_f32 v98, v98, v99
	v_cvt_pk_bf16_f32 v99, v104, v105
	global_store_dwordx4 v[108:109], v[96:99], off offset:256
	s_nop 0
	v_addc_co_u32_e32 v101, vcc, 0, v159, vcc
	v_lshlrev_b32_e32 v176, 16, v190
	v_and_b32_e32 v153, 0xffff0000, v193
	v_lshlrev_b32_e32 v152, 16, v193
	v_and_b32_e32 v155, 0xffff0000, v192
	v_lshlrev_b32_e32 v154, 16, v192
	v_pk_fma_f32 v[92:93], v[92:93], v[140:141], v[176:177]
	v_and_b32_e32 v127, 0xffff0000, v186
	v_lshlrev_b32_e32 v126, 16, v186
	v_and_b32_e32 v175, 0xffff0000, v191
	v_lshlrev_b32_e32 v174, 16, v191
	v_pk_fma_f32 v[152:153], v[90:91], v[138:139], v[152:153]
	v_pk_fma_f32 v[90:91], v[88:89], v[136:137], v[154:155]
	v_cvt_pk_bf16_f32 v88, v92, v93
	v_add_co_u32_e32 v92, vcc, s11, v156
	v_and_b32_e32 v121, 0xffff0000, v189
	v_lshlrev_b32_e32 v120, 16, v189
	v_and_b32_e32 v123, 0xffff0000, v188
	v_lshlrev_b32_e32 v122, 16, v188
	v_pk_fma_f32 v[94:95], v[94:95], v[142:143], v[174:175]
	v_addc_co_u32_e32 v93, vcc, 0, v157, vcc
	v_cvt_pk_bf16_f32 v89, v94, v95
	v_pk_fma_f32 v[84:85], v[84:85], v[132:133], v[126:127]
	v_and_b32_e32 v125, 0xffff0000, v187
	v_lshlrev_b32_e32 v124, 16, v187
	v_cvt_pk_bf16_f32 v90, v90, v91
	v_cvt_pk_bf16_f32 v91, v152, v153
	global_store_dwordx4 v[92:93], v[88:91], off
	s_waitcnt vmcnt(14)
	v_lshlrev_b32_e32 v104, 16, v210
	v_and_b32_e32 v105, 0xffff0000, v210
	v_pk_fma_f32 v[88:89], v[82:83], v[130:131], v[120:121]
	v_pk_fma_f32 v[82:83], v[80:81], v[128:129], v[122:123]
	v_cvt_pk_bf16_f32 v80, v84, v85
	v_add_co_u32_e32 v84, vcc, s62, v158
	v_pk_fma_f32 v[86:87], v[86:87], v[134:135], v[124:125]
	v_cvt_pk_bf16_f32 v82, v82, v83
	v_cvt_pk_bf16_f32 v83, v88, v89
	s_nop 0
	v_addc_co_u32_e32 v85, vcc, 0, v159, vcc
	v_cvt_pk_bf16_f32 v81, v86, v87
	global_store_dwordx4 v[92:93], v[80:83], off offset:256
	v_lshlrev_b32_e32 v108, 16, v212
	v_and_b32_e32 v109, 0xffff0000, v212
	v_lshlrev_b32_e32 v110, 16, v213
	v_and_b32_e32 v111, 0xffff0000, v213
	s_nop 0
	v_pk_fma_f32 v[76:77], v[76:77], v[140:141], v[104:105]
	v_lshlrev_b32_e32 v106, 16, v211
	v_and_b32_e32 v107, 0xffff0000, v211
	s_waitcnt vmcnt(14)
	v_lshlrev_b32_e32 v148, 16, v214
	v_and_b32_e32 v149, 0xffff0000, v214
	v_pk_fma_f32 v[104:105], v[74:75], v[138:139], v[110:111]
	v_pk_fma_f32 v[74:75], v[72:73], v[136:137], v[108:109]
	v_cvt_pk_bf16_f32 v72, v76, v77
	v_add_co_u32_e32 v76, vcc, s59, v156
	v_lshlrev_b32_e32 v150, 16, v216
	v_and_b32_e32 v151, 0xffff0000, v216
	v_lshlrev_b32_e32 v146, 16, v217
	v_and_b32_e32 v147, 0xffff0000, v217
	s_waitcnt vmcnt(13)
	v_and_b32_e32 v89, 0xffff0000, v221
	v_lshlrev_b32_e32 v88, 16, v221
	v_and_b32_e32 v91, 0xffff0000, v220
	v_lshlrev_b32_e32 v90, 16, v220
	v_and_b32_e32 v93, 0xffff0000, v219
	v_lshlrev_b32_e32 v92, 16, v219
	v_and_b32_e32 v95, 0xffff0000, v218
	v_lshlrev_b32_e32 v94, 16, v218
	s_waitcnt vmcnt(12)
	v_and_b32_e32 v113, 0xffff0000, v225
	v_lshlrev_b32_e32 v112, 16, v225
	v_and_b32_e32 v115, 0xffff0000, v224
	v_lshlrev_b32_e32 v114, 16, v224
	v_and_b32_e32 v119, 0xffff0000, v223
	v_lshlrev_b32_e32 v118, 16, v223
	v_pk_fma_f32 v[78:79], v[78:79], v[142:143], v[106:107]
	v_addc_co_u32_e32 v77, vcc, 0, v157, vcc
	v_cvt_pk_bf16_f32 v73, v78, v79
	v_pk_fma_f32 v[68:69], v[68:69], v[132:133], v[148:149]
	v_lshlrev_b32_e32 v144, 16, v215
	v_and_b32_e32 v145, 0xffff0000, v215
	v_cvt_pk_bf16_f32 v74, v74, v75
	v_cvt_pk_bf16_f32 v75, v104, v105
	global_store_dwordx4 v[76:77], v[72:75], off
	v_and_b32_e32 v117, 0xffff0000, v222
	v_lshlrev_b32_e32 v116, 16, v222
	v_pk_fma_f32 v[72:73], v[66:67], v[130:131], v[146:147]
	v_pk_fma_f32 v[66:67], v[64:65], v[128:129], v[150:151]
	v_cvt_pk_bf16_f32 v64, v68, v69
	v_pk_fma_f32 v[68:69], v[62:63], v[142:143], v[118:119]
	v_add_co_u32_e32 v62, vcc, s63, v158
	v_pk_fma_f32 v[70:71], v[70:71], v[134:135], v[144:145]
	v_cvt_pk_bf16_f32 v66, v66, v67
	v_cvt_pk_bf16_f32 v67, v72, v73
	s_nop 0
	v_addc_co_u32_e32 v63, vcc, 0, v159, vcc
	v_cvt_pk_bf16_f32 v65, v70, v71
	global_store_dwordx4 v[76:77], v[64:67], off offset:256
	s_waitcnt vmcnt(13)
	v_lshlrev_b32_e32 v70, 16, v226
	v_and_b32_e32 v71, 0xffff0000, v226
	v_lshlrev_b32_e32 v72, 16, v227
	v_and_b32_e32 v73, 0xffff0000, v227
	v_lshlrev_b32_e32 v74, 16, v228
	v_and_b32_e32 v75, 0xffff0000, v228
	v_lshlrev_b32_e32 v76, 16, v229
	v_and_b32_e32 v77, 0xffff0000, v229
	s_waitcnt vmcnt(12)
	v_lshlrev_b32_e32 v78, 16, v230
	v_and_b32_e32 v79, 0xffff0000, v230
	v_lshlrev_b32_e32 v96, 16, v231
	v_and_b32_e32 v97, 0xffff0000, v231
	v_lshlrev_b32_e32 v98, 16, v232
	v_and_b32_e32 v99, 0xffff0000, v232
	v_lshlrev_b32_e32 v100, 16, v233
	v_and_b32_e32 v101, 0xffff0000, v233
	v_pk_fma_f32 v[66:67], v[60:61], v[140:141], v[116:117]
	v_pk_fma_f32 v[102:103], v[58:59], v[138:139], v[112:113]
	s_nop 0
	v_pk_fma_f32 v[56:57], v[56:57], v[136:137], v[114:115]
	v_cvt_pk_bf16_f32 v66, v66, v67
	v_cvt_pk_bf16_f32 v67, v68, v69
	v_pk_fma_f32 v[48:49], v[48:49], v[140:141], v[70:71]
	v_cvt_pk_bf16_f32 v68, v56, v57
	v_add_co_u32_e32 v56, vcc, s60, v156
	v_pk_fma_f32 v[70:71], v[42:43], v[138:139], v[76:77]
	s_nop 0
	v_addc_co_u32_e32 v57, vcc, 0, v157, vcc
	v_pk_fma_f32 v[42:43], v[40:41], v[136:137], v[74:75]
	v_cvt_pk_bf16_f32 v40, v48, v49
	v_add_co_u32_e32 v48, vcc, s61, v156
	v_cvt_pk_bf16_f32 v69, v102, v103
	global_store_dwordx4 v[56:57], v[66:69], off
	v_pk_fma_f32 v[50:51], v[50:51], v[142:143], v[72:73]
	v_addc_co_u32_e32 v49, vcc, 0, v157, vcc
	v_pk_fma_f32 v[66:67], v[46:47], v[130:131], v[88:89]
	v_pk_fma_f32 v[46:47], v[44:45], v[128:129], v[90:91]
	v_cvt_pk_bf16_f32 v41, v50, v51
	v_pk_fma_f32 v[54:55], v[54:55], v[134:135], v[92:93]
	v_pk_fma_f32 v[52:53], v[52:53], v[132:133], v[94:95]
	v_cvt_pk_bf16_f32 v46, v46, v47
	v_cvt_pk_bf16_f32 v47, v66, v67
	v_cvt_pk_bf16_f32 v42, v42, v43
	v_cvt_pk_bf16_f32 v43, v70, v71
	global_store_dwordx4 v[48:49], v[40:43], off
	v_cvt_pk_bf16_f32 v44, v52, v53
	v_cvt_pk_bf16_f32 v45, v54, v55
	global_store_dwordx4 v[56:57], v[44:47], off offset:256
	s_waitcnt vmcnt(13)
	v_lshlrev_b32_e32 v52, 16, v239
	v_pk_fma_f32 v[40:41], v[26:27], v[130:131], v[100:101]
	v_pk_fma_f32 v[26:27], v[24:25], v[128:129], v[98:99]
	v_lshlrev_b32_e32 v46, 16, v238
	v_and_b32_e32 v47, 0xffff0000, v238
	v_and_b32_e32 v53, 0xffff0000, v239
	v_lshlrev_b32_e32 v54, 16, v240
	v_and_b32_e32 v55, 0xffff0000, v240
	v_pk_fma_f32 v[34:35], v[34:35], v[134:135], v[96:97]
	v_pk_fma_f32 v[32:33], v[32:33], v[132:133], v[78:79]
	v_cvt_pk_bf16_f32 v25, v34, v35
	v_cvt_pk_bf16_f32 v26, v26, v27
	v_cvt_pk_bf16_f32 v27, v40, v41
	v_pk_fma_f32 v[28:29], v[28:29], v[136:137], v[54:55]
	v_cvt_pk_bf16_f32 v24, v32, v33
	global_store_dwordx4 v[48:49], v[24:27], off offset:256
	v_lshlrev_b32_e32 v56, 16, v241
	v_and_b32_e32 v57, 0xffff0000, v241
	v_pk_fma_f32 v[26:27], v[38:39], v[142:143], v[52:53]
	v_pk_fma_f32 v[24:25], v[36:37], v[140:141], v[46:47]
	v_and_b32_e32 v45, 0xffff0000, v237
	v_cvt_pk_bf16_f32 v24, v24, v25
	v_cvt_pk_bf16_f32 v25, v26, v27
	v_cvt_pk_bf16_f32 v26, v28, v29
	v_add_co_u32_e32 v28, vcc, s62, v156
	v_lshlrev_b32_e32 v66, 16, v234
	v_and_b32_e32 v67, 0xffff0000, v234
	v_lshlrev_b32_e32 v68, 16, v235
	v_and_b32_e32 v69, 0xffff0000, v235
	v_lshlrev_b32_e32 v80, 16, v236
	v_and_b32_e32 v81, 0xffff0000, v236
	v_lshlrev_b32_e32 v44, 16, v237
	v_pk_fma_f32 v[30:31], v[30:31], v[138:139], v[56:57]
	v_addc_co_u32_e32 v29, vcc, 0, v157, vcc
	v_cvt_pk_bf16_f32 v27, v30, v31
	global_store_dwordx4 v[28:29], v[24:27], off
	v_pk_fma_f32 v[22:23], v[22:23], v[134:135], v[68:69]
	v_pk_fma_f32 v[20:21], v[20:21], v[132:133], v[66:67]
	v_pk_fma_f32 v[24:25], v[18:19], v[130:131], v[44:45]
	v_pk_fma_f32 v[18:19], v[16:17], v[128:129], v[80:81]
	v_cvt_pk_bf16_f32 v16, v20, v21
	v_cvt_pk_bf16_f32 v17, v22, v23
	s_waitcnt vmcnt(14)
	v_and_b32_e32 v31, 0xffff0000, v242
	v_lshlrev_b32_e32 v30, 16, v242
	v_cvt_pk_bf16_f32 v18, v18, v19
	v_cvt_pk_bf16_f32 v19, v24, v25
	v_and_b32_e32 v25, 0xffff0000, v245
	v_lshlrev_b32_e32 v24, 16, v245
	v_and_b32_e32 v27, 0xffff0000, v244
	v_lshlrev_b32_e32 v26, 16, v244
	v_pk_fma_f32 v[12:13], v[12:13], v[140:141], v[30:31]
	global_store_dwordx4 v[28:29], v[16:19], off offset:256
	v_and_b32_e32 v29, 0xffff0000, v243
	v_lshlrev_b32_e32 v28, 16, v243
	v_pk_fma_f32 v[24:25], v[10:11], v[138:139], v[24:25]
	v_pk_fma_f32 v[10:11], v[8:9], v[136:137], v[26:27]
	v_cvt_pk_bf16_f32 v8, v12, v13
	v_add_co_u32_e32 v12, vcc, s63, v156
	s_waitcnt vmcnt(14)
	v_and_b32_e32 v17, 0xffff0000, v249
	v_lshlrev_b32_e32 v16, 16, v249
	v_and_b32_e32 v19, 0xffff0000, v248
	v_lshlrev_b32_e32 v18, 16, v248
	v_pk_fma_f32 v[14:15], v[14:15], v[142:143], v[28:29]
	v_addc_co_u32_e32 v13, vcc, 0, v157, vcc
	v_cvt_pk_bf16_f32 v9, v14, v15
	v_and_b32_e32 v21, 0xffff0000, v247
	v_lshlrev_b32_e32 v20, 16, v247
	v_and_b32_e32 v23, 0xffff0000, v246
	v_lshlrev_b32_e32 v22, 16, v246
	v_cvt_pk_bf16_f32 v10, v10, v11
	v_cvt_pk_bf16_f32 v11, v24, v25
	global_store_dwordx4 v[12:13], v[8:11], off
	s_andn2_b64 vcc, exec, s[4:5]
	s_mov_b64 s[4:5], -1
	v_pk_fma_f32 v[8:9], v[2:3], v[130:131], v[16:17]
	v_pk_fma_f32 v[2:3], v[0:1], v[128:129], v[18:19]
	v_pk_fma_f32 v[6:7], v[6:7], v[134:135], v[20:21]
	v_pk_fma_f32 v[4:5], v[4:5], v[132:133], v[22:23]
	v_cvt_pk_bf16_f32 v1, v6, v7
	v_cvt_pk_bf16_f32 v2, v2, v3
	v_cvt_pk_bf16_f32 v3, v8, v9
	s_nop 0
	v_cvt_pk_bf16_f32 v0, v4, v5
	global_store_dwordx4 v[12:13], v[0:3], off offset:256
	s_cbranch_vccnz .LBB0_2132
	s_andn2_b64 vcc, exec, s[18:19]
	s_cbranch_vccnz .LBB0_2131
	s_barrier
	s_branch .LBB0_2131
